# combo7 + phase 0: w_in column-max loops issue all 32 loads before reducing; rows per workgroup 37 / 104 instead of 32 / 111
# baseline (speedup 1.0000x reference)
.LBB0_9:
	v_lshl_add_u64 v[36:37], v[22:23], 0, s[6:7]
	v_add_co_u32_e32 v28, vcc, 0x9000, v36
	global_load_dwordx4 v[80:83], v[36:37], off
	s_nop 0
	v_addc_co_u32_e32 v29, vcc, 0, v37, vcc
	v_add_co_u32_e32 v46, vcc, 0x13000, v36
	global_load_dwordx4 v[84:87], v[28:29], off offset:2080
	s_nop 0
	v_addc_co_u32_e32 v47, vcc, 0, v37, vcc
	v_add_co_u32_e32 v48, vcc, 0x1c000, v36
	s_add_u32 s6, s6, 0x260800
	s_nop 0
	v_addc_co_u32_e32 v49, vcc, 0, v37, vcc
	v_add_co_u32_e32 v54, vcc, 0x26000, v36
	global_load_dwordx4 v[88:91], v[46:47], off offset:64
	global_load_dwordx4 v[92:95], v[48:49], off offset:2144
	v_addc_co_u32_e32 v55, vcc, 0, v37, vcc
	v_add_co_u32_e32 v56, vcc, 0x2f000, v36
	s_addc_u32 s7, s7, 0
	s_nop 0
	v_addc_co_u32_e32 v57, vcc, 0, v37, vcc
	v_add_co_u32_e32 v62, vcc, 0x39000, v36
	global_load_dwordx4 v[96:99], v[54:55], off offset:128
	global_load_dwordx4 v[100:103], v[56:57], off offset:2208
	v_addc_co_u32_e32 v63, vcc, 0, v37, vcc
	v_add_co_u32_e32 v36, vcc, 0x42000, v36
	s_nop 0
	v_addc_co_u32_e32 v37, vcc, 0, v37, vcc
	global_load_dwordx4 v[104:107], v[62:63], off offset:192
	global_load_dwordx4 v[108:111], v[36:37], off offset:2272
	v_lshl_add_u64 v[36:37], v[22:23], 0, s[6:7]
	v_add_co_u32_e32 v28, vcc, 0x9000, v36
	global_load_dwordx4 v[112:115], v[36:37], off
	s_nop 0
	v_addc_co_u32_e32 v29, vcc, 0, v37, vcc
	v_add_co_u32_e32 v46, vcc, 0x13000, v36
	global_load_dwordx4 v[116:119], v[28:29], off offset:2080
	s_nop 0
	v_addc_co_u32_e32 v47, vcc, 0, v37, vcc
	v_add_co_u32_e32 v48, vcc, 0x1c000, v36
	s_add_u32 s6, s6, 0x260800
	s_nop 0
	v_addc_co_u32_e32 v49, vcc, 0, v37, vcc
	v_add_co_u32_e32 v54, vcc, 0x26000, v36
	global_load_dwordx4 v[120:123], v[46:47], off offset:64
	global_load_dwordx4 v[124:127], v[48:49], off offset:2144
	v_addc_co_u32_e32 v55, vcc, 0, v37, vcc
	v_add_co_u32_e32 v56, vcc, 0x2f000, v36
	s_addc_u32 s7, s7, 0
	s_nop 0
	v_addc_co_u32_e32 v57, vcc, 0, v37, vcc
	v_add_co_u32_e32 v62, vcc, 0x39000, v36
	global_load_dwordx4 v[128:131], v[54:55], off offset:128
	global_load_dwordx4 v[132:135], v[56:57], off offset:2208
	v_addc_co_u32_e32 v63, vcc, 0, v37, vcc
	v_add_co_u32_e32 v36, vcc, 0x42000, v36
	s_nop 0
	v_addc_co_u32_e32 v37, vcc, 0, v37, vcc
	global_load_dwordx4 v[136:139], v[62:63], off offset:192
	global_load_dwordx4 v[140:143], v[36:37], off offset:2272
	v_lshl_add_u64 v[36:37], v[22:23], 0, s[6:7]
	v_add_co_u32_e32 v28, vcc, 0x9000, v36
	global_load_dwordx4 v[144:147], v[36:37], off
	s_nop 0
	v_addc_co_u32_e32 v29, vcc, 0, v37, vcc
	v_add_co_u32_e32 v46, vcc, 0x13000, v36
	global_load_dwordx4 v[148:151], v[28:29], off offset:2080
	s_nop 0
	v_addc_co_u32_e32 v47, vcc, 0, v37, vcc
	v_add_co_u32_e32 v48, vcc, 0x1c000, v36
	s_add_u32 s6, s6, 0x260800
	s_nop 0
	v_addc_co_u32_e32 v49, vcc, 0, v37, vcc
	v_add_co_u32_e32 v54, vcc, 0x26000, v36
	global_load_dwordx4 v[152:155], v[46:47], off offset:64
	global_load_dwordx4 v[156:159], v[48:49], off offset:2144
	v_addc_co_u32_e32 v55, vcc, 0, v37, vcc
	v_add_co_u32_e32 v56, vcc, 0x2f000, v36
	s_addc_u32 s7, s7, 0
	s_nop 0
	v_addc_co_u32_e32 v57, vcc, 0, v37, vcc
	v_add_co_u32_e32 v62, vcc, 0x39000, v36
	global_load_dwordx4 v[160:163], v[54:55], off offset:128
	global_load_dwordx4 v[164:167], v[56:57], off offset:2208
	v_addc_co_u32_e32 v63, vcc, 0, v37, vcc
	v_add_co_u32_e32 v36, vcc, 0x42000, v36
	s_nop 0
	v_addc_co_u32_e32 v37, vcc, 0, v37, vcc
	global_load_dwordx4 v[168:171], v[62:63], off offset:192
	global_load_dwordx4 v[172:175], v[36:37], off offset:2272
	v_lshl_add_u64 v[36:37], v[22:23], 0, s[6:7]
	v_add_co_u32_e32 v28, vcc, 0x9000, v36
	global_load_dwordx4 v[176:179], v[36:37], off
	s_nop 0
	v_addc_co_u32_e32 v29, vcc, 0, v37, vcc
	v_add_co_u32_e32 v46, vcc, 0x13000, v36
	global_load_dwordx4 v[180:183], v[28:29], off offset:2080
	s_nop 0
	v_addc_co_u32_e32 v47, vcc, 0, v37, vcc
	v_add_co_u32_e32 v48, vcc, 0x1c000, v36
	s_add_u32 s6, s6, 0x260800
	s_nop 0
	v_addc_co_u32_e32 v49, vcc, 0, v37, vcc
	v_add_co_u32_e32 v54, vcc, 0x26000, v36
	global_load_dwordx4 v[184:187], v[46:47], off offset:64
	global_load_dwordx4 v[188:191], v[48:49], off offset:2144
	v_addc_co_u32_e32 v55, vcc, 0, v37, vcc
	v_add_co_u32_e32 v56, vcc, 0x2f000, v36
	s_addc_u32 s7, s7, 0
	s_nop 0
	v_addc_co_u32_e32 v57, vcc, 0, v37, vcc
	v_add_co_u32_e32 v62, vcc, 0x39000, v36
	global_load_dwordx4 v[192:195], v[54:55], off offset:128
	global_load_dwordx4 v[196:199], v[56:57], off offset:2208
	v_addc_co_u32_e32 v63, vcc, 0, v37, vcc
	v_add_co_u32_e32 v36, vcc, 0x42000, v36
	s_nop 0
	v_addc_co_u32_e32 v37, vcc, 0, v37, vcc
	global_load_dwordx4 v[200:203], v[62:63], off offset:192
	global_load_dwordx4 v[204:207], v[36:37], off offset:2272
	s_waitcnt vmcnt(30)
	v_max3_f32 v9, v13, |v80|, |v84|
	v_max3_f32 v11, v19, |v81|, |v85|
	v_max3_f32 v13, v17, |v82|, |v86|
	v_max3_f32 v15, v15, |v83|, |v87|
	s_waitcnt vmcnt(28)
	v_max3_f32 v9, v9, |v88|, |v92|
	v_max3_f32 v11, v11, |v89|, |v93|
	v_max3_f32 v13, v13, |v90|, |v94|
	v_max3_f32 v15, v15, |v91|, |v95|
	s_waitcnt vmcnt(26)
	v_max3_f32 v9, v9, |v96|, |v100|
	v_max3_f32 v11, v11, |v97|, |v101|
	v_max3_f32 v17, v13, |v98|, |v102|
	v_max3_f32 v15, v15, |v99|, |v103|
	s_waitcnt vmcnt(24)
	v_max3_f32 v13, v9, |v104|, |v108|
	v_max3_f32 v19, v11, |v105|, |v109|
	v_max3_f32 v17, v17, |v106|, |v110|
	v_max3_f32 v15, v15, |v107|, |v111|
	s_waitcnt vmcnt(22)
	v_max3_f32 v9, v13, |v112|, |v116|
	v_max3_f32 v11, v19, |v113|, |v117|
	v_max3_f32 v13, v17, |v114|, |v118|
	v_max3_f32 v15, v15, |v115|, |v119|
	s_waitcnt vmcnt(20)
	v_max3_f32 v9, v9, |v120|, |v124|
	v_max3_f32 v11, v11, |v121|, |v125|
	v_max3_f32 v13, v13, |v122|, |v126|
	v_max3_f32 v15, v15, |v123|, |v127|
	s_waitcnt vmcnt(18)
	v_max3_f32 v9, v9, |v128|, |v132|
	v_max3_f32 v11, v11, |v129|, |v133|
	v_max3_f32 v17, v13, |v130|, |v134|
	v_max3_f32 v15, v15, |v131|, |v135|
	s_waitcnt vmcnt(16)
	v_max3_f32 v13, v9, |v136|, |v140|
	v_max3_f32 v19, v11, |v137|, |v141|
	v_max3_f32 v17, v17, |v138|, |v142|
	v_max3_f32 v15, v15, |v139|, |v143|
	s_waitcnt vmcnt(14)
	v_max3_f32 v9, v13, |v144|, |v148|
	v_max3_f32 v11, v19, |v145|, |v149|
	v_max3_f32 v13, v17, |v146|, |v150|
	v_max3_f32 v15, v15, |v147|, |v151|
	s_waitcnt vmcnt(12)
	v_max3_f32 v9, v9, |v152|, |v156|
	v_max3_f32 v11, v11, |v153|, |v157|
	v_max3_f32 v13, v13, |v154|, |v158|
	v_max3_f32 v15, v15, |v155|, |v159|
	s_waitcnt vmcnt(10)
	v_max3_f32 v9, v9, |v160|, |v164|
	v_max3_f32 v11, v11, |v161|, |v165|
	v_max3_f32 v17, v13, |v162|, |v166|
	v_max3_f32 v15, v15, |v163|, |v167|
	s_waitcnt vmcnt(8)
	v_max3_f32 v13, v9, |v168|, |v172|
	v_max3_f32 v19, v11, |v169|, |v173|
	v_max3_f32 v17, v17, |v170|, |v174|
	v_max3_f32 v15, v15, |v171|, |v175|
	s_waitcnt vmcnt(6)
	v_max3_f32 v9, v13, |v176|, |v180|
	v_max3_f32 v11, v19, |v177|, |v181|
	v_max3_f32 v13, v17, |v178|, |v182|
	v_max3_f32 v15, v15, |v179|, |v183|
	s_waitcnt vmcnt(4)
	v_max3_f32 v9, v9, |v184|, |v188|
	v_max3_f32 v11, v11, |v185|, |v189|
	v_max3_f32 v13, v13, |v186|, |v190|
	v_max3_f32 v15, v15, |v187|, |v191|
	s_waitcnt vmcnt(2)
	v_max3_f32 v9, v9, |v192|, |v196|
	v_max3_f32 v11, v11, |v193|, |v197|
	v_max3_f32 v17, v13, |v194|, |v198|
	v_max3_f32 v15, v15, |v195|, |v199|
	s_waitcnt vmcnt(0)
	v_max3_f32 v13, v9, |v200|, |v204|
	v_max3_f32 v19, v11, |v201|, |v205|
	v_max3_f32 v17, v17, |v202|, |v206|
	v_max3_f32 v15, v15, |v203|, |v207|
	v_and_b32_e32 v11, 64, v40
	v_xor_b32_e32 v9, 8, v40
	v_add_u32_e32 v21, 64, v11
	v_cmp_lt_i32_e32 vcc, v9, v21
	v_xor_b32_e32 v11, 16, v40
	s_nop 0
	v_cndmask_b32_e32 v9, v40, v9, vcc
	v_lshlrev_b32_e32 v9, 2, v9
	ds_bpermute_b32 v24, v9, v13
	v_cmp_lt_i32_e32 vcc, v11, v21
	v_max_f32_e32 v13, v13, v13
	s_waitcnt lgkmcnt(0)
	v_max_f32_e32 v24, v24, v24
	v_cndmask_b32_e32 v11, v40, v11, vcc
	v_lshlrev_b32_e32 v11, 2, v11
	v_max_f32_e32 v24, v13, v24
	ds_bpermute_b32 v25, v11, v24
	v_xor_b32_e32 v13, 32, v40
	v_cmp_lt_i32_e32 vcc, v13, v21
	s_waitcnt lgkmcnt(0)
	v_max_f32_e32 v21, v25, v25
	v_cndmask_b32_e32 v13, v40, v13, vcc
	v_lshlrev_b32_e32 v13, 2, v13
	v_max_f32_e32 v21, v24, v21
	ds_bpermute_b32 v24, v13, v21
	s_and_saveexec_b64 s[6:7], s[4:5]
	s_cbranch_execz .LBB0_12
	s_waitcnt lgkmcnt(0)
	v_max_f32_e32 v24, v24, v24
	v_max_f32_e32 v21, v21, v21
	v_max_f32_e32 v21, v21, v24
	ds_write_b32 v39, v21

.LBB0_19:
	v_lshl_add_u64 v[36:37], v[22:23], 0, s[6:7]
	v_add_co_u32_e32 v28, vcc, 0x9000, v36
	global_load_dwordx4 v[80:83], v[36:37], off offset:128
	s_nop 0
	v_addc_co_u32_e32 v29, vcc, 0, v37, vcc
	v_add_co_u32_e32 v46, vcc, 0x13000, v36
	global_load_dwordx4 v[84:87], v[28:29], off offset:2208
	s_nop 0
	v_addc_co_u32_e32 v47, vcc, 0, v37, vcc
	v_add_co_u32_e32 v48, vcc, 0x1c000, v36
	s_add_u32 s6, s6, 0x260800
	s_nop 0
	v_addc_co_u32_e32 v49, vcc, 0, v37, vcc
	v_add_co_u32_e32 v54, vcc, 0x26000, v36
	global_load_dwordx4 v[88:91], v[46:47], off offset:192
	global_load_dwordx4 v[92:95], v[48:49], off offset:2272
	v_addc_co_u32_e32 v55, vcc, 0, v37, vcc
	v_add_co_u32_e32 v56, vcc, 0x2f000, v36
	s_addc_u32 s7, s7, 0
	s_nop 0
	v_addc_co_u32_e32 v57, vcc, 0, v37, vcc
	v_add_co_u32_e32 v62, vcc, 0x39000, v36
	global_load_dwordx4 v[96:99], v[54:55], off offset:256
	global_load_dwordx4 v[100:103], v[56:57], off offset:2336
	v_addc_co_u32_e32 v63, vcc, 0, v37, vcc
	v_add_co_u32_e32 v36, vcc, 0x42000, v36
	s_nop 0
	v_addc_co_u32_e32 v37, vcc, 0, v37, vcc
	global_load_dwordx4 v[104:107], v[62:63], off offset:320
	global_load_dwordx4 v[108:111], v[36:37], off offset:2400
	v_lshl_add_u64 v[36:37], v[22:23], 0, s[6:7]
	v_add_co_u32_e32 v28, vcc, 0x9000, v36
	global_load_dwordx4 v[112:115], v[36:37], off offset:128
	s_nop 0
	v_addc_co_u32_e32 v29, vcc, 0, v37, vcc
	v_add_co_u32_e32 v46, vcc, 0x13000, v36
	global_load_dwordx4 v[116:119], v[28:29], off offset:2208
	s_nop 0
	v_addc_co_u32_e32 v47, vcc, 0, v37, vcc
	v_add_co_u32_e32 v48, vcc, 0x1c000, v36
	s_add_u32 s6, s6, 0x260800
	s_nop 0
	v_addc_co_u32_e32 v49, vcc, 0, v37, vcc
	v_add_co_u32_e32 v54, vcc, 0x26000, v36
	global_load_dwordx4 v[120:123], v[46:47], off offset:192
	global_load_dwordx4 v[124:127], v[48:49], off offset:2272
	v_addc_co_u32_e32 v55, vcc, 0, v37, vcc
	v_add_co_u32_e32 v56, vcc, 0x2f000, v36
	s_addc_u32 s7, s7, 0
	s_nop 0
	v_addc_co_u32_e32 v57, vcc, 0, v37, vcc
	v_add_co_u32_e32 v62, vcc, 0x39000, v36
	global_load_dwordx4 v[128:131], v[54:55], off offset:256
	global_load_dwordx4 v[132:135], v[56:57], off offset:2336
	v_addc_co_u32_e32 v63, vcc, 0, v37, vcc
	v_add_co_u32_e32 v36, vcc, 0x42000, v36
	s_nop 0
	v_addc_co_u32_e32 v37, vcc, 0, v37, vcc
	global_load_dwordx4 v[136:139], v[62:63], off offset:320
	global_load_dwordx4 v[140:143], v[36:37], off offset:2400
	v_lshl_add_u64 v[36:37], v[22:23], 0, s[6:7]
	v_add_co_u32_e32 v28, vcc, 0x9000, v36
	global_load_dwordx4 v[144:147], v[36:37], off offset:128
	s_nop 0
	v_addc_co_u32_e32 v29, vcc, 0, v37, vcc
	v_add_co_u32_e32 v46, vcc, 0x13000, v36
	global_load_dwordx4 v[148:151], v[28:29], off offset:2208
	s_nop 0
	v_addc_co_u32_e32 v47, vcc, 0, v37, vcc
	v_add_co_u32_e32 v48, vcc, 0x1c000, v36
	s_add_u32 s6, s6, 0x260800
	s_nop 0
	v_addc_co_u32_e32 v49, vcc, 0, v37, vcc
	v_add_co_u32_e32 v54, vcc, 0x26000, v36
	global_load_dwordx4 v[152:155], v[46:47], off offset:192
	global_load_dwordx4 v[156:159], v[48:49], off offset:2272
	v_addc_co_u32_e32 v55, vcc, 0, v37, vcc
	v_add_co_u32_e32 v56, vcc, 0x2f000, v36
	s_addc_u32 s7, s7, 0
	s_nop 0
	v_addc_co_u32_e32 v57, vcc, 0, v37, vcc
	v_add_co_u32_e32 v62, vcc, 0x39000, v36
	global_load_dwordx4 v[160:163], v[54:55], off offset:256
	global_load_dwordx4 v[164:167], v[56:57], off offset:2336
	v_addc_co_u32_e32 v63, vcc, 0, v37, vcc
	v_add_co_u32_e32 v36, vcc, 0x42000, v36
	s_nop 0
	v_addc_co_u32_e32 v37, vcc, 0, v37, vcc
	global_load_dwordx4 v[168:171], v[62:63], off offset:320
	global_load_dwordx4 v[172:175], v[36:37], off offset:2400
	v_lshl_add_u64 v[36:37], v[22:23], 0, s[6:7]
	v_add_co_u32_e32 v28, vcc, 0x9000, v36
	global_load_dwordx4 v[176:179], v[36:37], off offset:128
	s_nop 0
	v_addc_co_u32_e32 v29, vcc, 0, v37, vcc
	v_add_co_u32_e32 v46, vcc, 0x13000, v36
	global_load_dwordx4 v[180:183], v[28:29], off offset:2208
	s_nop 0
	v_addc_co_u32_e32 v47, vcc, 0, v37, vcc
	v_add_co_u32_e32 v48, vcc, 0x1c000, v36
	s_add_u32 s6, s6, 0x260800
	s_nop 0
	v_addc_co_u32_e32 v49, vcc, 0, v37, vcc
	v_add_co_u32_e32 v54, vcc, 0x26000, v36
	global_load_dwordx4 v[184:187], v[46:47], off offset:192
	global_load_dwordx4 v[188:191], v[48:49], off offset:2272
	v_addc_co_u32_e32 v55, vcc, 0, v37, vcc
	v_add_co_u32_e32 v56, vcc, 0x2f000, v36
	s_addc_u32 s7, s7, 0
	s_nop 0
	v_addc_co_u32_e32 v57, vcc, 0, v37, vcc
	v_add_co_u32_e32 v62, vcc, 0x39000, v36
	global_load_dwordx4 v[192:195], v[54:55], off offset:256
	global_load_dwordx4 v[196:199], v[56:57], off offset:2336
	v_addc_co_u32_e32 v63, vcc, 0, v37, vcc
	v_add_co_u32_e32 v36, vcc, 0x42000, v36
	s_nop 0
	v_addc_co_u32_e32 v37, vcc, 0, v37, vcc
	global_load_dwordx4 v[200:203], v[62:63], off offset:320
	global_load_dwordx4 v[204:207], v[36:37], off offset:2400
	s_waitcnt vmcnt(30)
	v_max3_f32 v21, v21, |v80|, |v84|
	v_max3_f32 v19, v19, |v81|, |v85|
	v_max3_f32 v17, v17, |v82|, |v86|
	v_max3_f32 v15, v15, |v83|, |v87|
	s_waitcnt vmcnt(28)
	v_max3_f32 v21, v21, |v88|, |v92|
	v_max3_f32 v19, v19, |v89|, |v93|
	v_max3_f32 v17, v17, |v90|, |v94|
	v_max3_f32 v15, v15, |v91|, |v95|
	s_waitcnt vmcnt(26)
	v_max3_f32 v21, v21, |v96|, |v100|
	v_max3_f32 v19, v19, |v97|, |v101|
	v_max3_f32 v17, v17, |v98|, |v102|
	v_max3_f32 v15, v15, |v99|, |v103|
	s_waitcnt vmcnt(24)
	v_max3_f32 v21, v21, |v104|, |v108|
	v_max3_f32 v19, v19, |v105|, |v109|
	v_max3_f32 v17, v17, |v106|, |v110|
	v_max3_f32 v15, v15, |v107|, |v111|
	s_waitcnt vmcnt(22)
	v_max3_f32 v21, v21, |v112|, |v116|
	v_max3_f32 v19, v19, |v113|, |v117|
	v_max3_f32 v17, v17, |v114|, |v118|
	v_max3_f32 v15, v15, |v115|, |v119|
	s_waitcnt vmcnt(20)
	v_max3_f32 v21, v21, |v120|, |v124|
	v_max3_f32 v19, v19, |v121|, |v125|
	v_max3_f32 v17, v17, |v122|, |v126|
	v_max3_f32 v15, v15, |v123|, |v127|
	s_waitcnt vmcnt(18)
	v_max3_f32 v21, v21, |v128|, |v132|
	v_max3_f32 v19, v19, |v129|, |v133|
	v_max3_f32 v17, v17, |v130|, |v134|
	v_max3_f32 v15, v15, |v131|, |v135|
	s_waitcnt vmcnt(16)
	v_max3_f32 v21, v21, |v136|, |v140|
	v_max3_f32 v19, v19, |v137|, |v141|
	v_max3_f32 v17, v17, |v138|, |v142|
	v_max3_f32 v15, v15, |v139|, |v143|
	s_waitcnt vmcnt(14)
	v_max3_f32 v21, v21, |v144|, |v148|
	v_max3_f32 v19, v19, |v145|, |v149|
	v_max3_f32 v17, v17, |v146|, |v150|
	v_max3_f32 v15, v15, |v147|, |v151|
	s_waitcnt vmcnt(12)
	v_max3_f32 v21, v21, |v152|, |v156|
	v_max3_f32 v19, v19, |v153|, |v157|
	v_max3_f32 v17, v17, |v154|, |v158|
	v_max3_f32 v15, v15, |v155|, |v159|
	s_waitcnt vmcnt(10)
	v_max3_f32 v21, v21, |v160|, |v164|
	v_max3_f32 v19, v19, |v161|, |v165|
	v_max3_f32 v17, v17, |v162|, |v166|
	v_max3_f32 v15, v15, |v163|, |v167|
	s_waitcnt vmcnt(8)
	v_max3_f32 v21, v21, |v168|, |v172|
	v_max3_f32 v19, v19, |v169|, |v173|
	v_max3_f32 v17, v17, |v170|, |v174|
	v_max3_f32 v15, v15, |v171|, |v175|
	s_waitcnt vmcnt(6)
	v_max3_f32 v21, v21, |v176|, |v180|
	v_max3_f32 v19, v19, |v177|, |v181|
	v_max3_f32 v17, v17, |v178|, |v182|
	v_max3_f32 v15, v15, |v179|, |v183|
	s_waitcnt vmcnt(4)
	v_max3_f32 v21, v21, |v184|, |v188|
	v_max3_f32 v19, v19, |v185|, |v189|
	v_max3_f32 v17, v17, |v186|, |v190|
	v_max3_f32 v15, v15, |v187|, |v191|
	s_waitcnt vmcnt(2)
	v_max3_f32 v21, v21, |v192|, |v196|
	v_max3_f32 v19, v19, |v193|, |v197|
	v_max3_f32 v17, v17, |v194|, |v198|
	v_max3_f32 v15, v15, |v195|, |v199|
	s_waitcnt vmcnt(0)
	v_max3_f32 v21, v21, |v200|, |v204|
	v_max3_f32 v19, v19, |v201|, |v205|
	v_max3_f32 v17, v17, |v202|, |v206|
	v_max3_f32 v15, v15, |v203|, |v207|
	ds_bpermute_b32 v24, v9, v21
	v_max_f32_e32 v21, v21, v21
	s_waitcnt lgkmcnt(0)
	v_max_f32_e32 v24, v24, v24
	v_max_f32_e32 v21, v21, v24
	ds_bpermute_b32 v24, v11, v21
	s_waitcnt lgkmcnt(0)
	v_max_f32_e32 v24, v24, v24
	v_max_f32_e32 v21, v21, v24
	ds_bpermute_b32 v24, v13, v21
	s_and_saveexec_b64 s[6:7], s[4:5]
	s_cbranch_execz .LBB0_22
	s_waitcnt lgkmcnt(0)
	v_max_f32_e32 v24, v24, v24
	v_max_f32_e32 v21, v21, v21
	v_max_f32_e32 v21, v21, v24
	ds_write_b32 v39, v21 offset:128

.LBB0_50:
	v_mul_u32_u24_e32 v1, 0x2608, v0
	v_lshlrev_b32_e32 v34, 2, v1
	v_mov_b32_e32 v35, 0
	s_waitcnt lgkmcnt(0)
	v_lshl_add_u64 v[26:27], s[6:7], 0, v[34:35]
	v_add_co_u32_e32 v12, vcc, 0x4000, v26
	s_mov_b64 s[4:5], 0x4000
	s_nop 0
	v_addc_co_u32_e32 v13, vcc, 0, v27, vcc
	v_add_co_u32_e32 v20, vcc, 0x1308000, v26
	v_lshl_add_u64 v[10:11], v[26:27], 0, s[4:5]
	s_nop 0
	v_addc_co_u32_e32 v21, vcc, 0, v27, vcc
	v_add_co_u32_e32 v30, vcc, 0x260c000, v26
	s_mov_b64 s[4:5], 0x1308000
	s_nop 0
	v_addc_co_u32_e32 v31, vcc, 0, v27, vcc
	v_lshl_add_u64 v[18:19], v[26:27], 0, s[4:5]
	s_mov_b64 s[4:5], 0x260c000
	v_add_co_u32_e32 v38, vcc, 0x3910000, v26
	v_lshl_add_u64 v[28:29], v[26:27], 0, s[4:5]
	s_mov_b64 s[4:5], 0x3910000
	v_addc_co_u32_e32 v39, vcc, 0, v27, vcc
	global_load_dwordx4 v[2:5], v[12:13], off
	global_load_dwordx4 v[6:9], v[10:11], off offset:16
	s_nop 0
	global_load_dwordx4 v[10:13], v[20:21], off
	global_load_dwordx4 v[14:17], v[18:19], off offset:16
	s_nop 0
	global_load_dwordx4 v[18:21], v[30:31], off
	global_load_dwordx4 v[22:25], v[28:29], off offset:16
	v_lshl_add_u64 v[36:37], v[26:27], 0, s[4:5]
	global_load_dwordx4 v[26:29], v[38:39], off
	global_load_dwordx4 v[30:33], v[36:37], off offset:16
	v_lshl_add_u32 v1, v0, 2, 0
	v_mov_b32_e32 v36, v0
	s_cmpk_eq_i32 s3, 0x100
	s_movk_i32 s44, 0x4000
	s_mov_b32 s10, 0
	s_waitcnt vmcnt(5)
	ds_write2st64_b32 v1, v2, v10 offset1:8
	s_waitcnt vmcnt(4)
	ds_write2st64_b32 v1, v6, v14 offset0:128 offset1:136
	ds_write2st64_b32 v1, v3, v11 offset0:32 offset1:40
	ds_write2st64_b32 v1, v7, v15 offset0:160 offset1:168
	ds_write2st64_b32 v1, v4, v12 offset0:64 offset1:72
	ds_write2st64_b32 v1, v8, v16 offset0:192 offset1:200
	ds_write2st64_b32 v1, v5, v13 offset0:96 offset1:104
	ds_write2st64_b32 v1, v9, v17 offset0:224 offset1:232
	s_waitcnt vmcnt(1)
	ds_write2st64_b32 v1, v18, v26 offset0:16 offset1:24
	s_waitcnt vmcnt(0)
	ds_write2st64_b32 v1, v22, v30 offset0:144 offset1:152
	ds_write2st64_b32 v1, v19, v27 offset0:48 offset1:56
	ds_write2st64_b32 v1, v23, v31 offset0:176 offset1:184
	ds_write2st64_b32 v1, v20, v28 offset0:80 offset1:88
	ds_write2st64_b32 v1, v24, v32 offset0:208 offset1:216
	ds_write2st64_b32 v1, v21, v29 offset0:112 offset1:120
	ds_write2st64_b32 v1, v25, v33 offset0:240 offset1:248
	s_waitcnt lgkmcnt(0)
	s_barrier
	s_load_dwordx4 s[4:7], s[0:1], 0x0
	v_and_b32_e32 v37, 63, v36
	v_lshlrev_b32_e32 v34, 4, v37
	s_waitcnt lgkmcnt(0)
	global_load_dwordx4 v[2:5], v34, s[6:7]
	global_load_dwordx4 v[6:9], v34, s[6:7] offset:1024
	global_load_dwordx4 v[10:13], v34, s[6:7] offset:2048
	global_load_dwordx4 v[14:17], v34, s[6:7] offset:3072
	v_lshl_add_u64 v[18:19], s[6:7], 0, v[34:35]
	v_add_co_u32_e32 v38, vcc, 0x1000, v18
	s_cselect_b64 s[6:7], -1, 0
	s_nop 0
	v_addc_co_u32_e32 v39, vcc, 0, v19, vcc
	global_load_dwordx4 v[18:21], v[38:39], off
	global_load_dwordx4 v[22:25], v[38:39], off offset:1024
	global_load_dwordx4 v[26:29], v[38:39], off offset:2048
	global_load_dwordx4 v[30:33], v[38:39], off offset:3072
	s_and_b64 vcc, exec, s[6:7]
	s_cbranch_vccz .LBB0_55
	s_and_b64 vcc, exec, s[14:15]
	s_cbranch_vccz .LBB0_53
	s_mul_i32 s8, s2, 104
	s_add_i32 s10, s8, 0xffffd838
	s_cbranch_execz .LBB0_54
	s_branch .LBB0_55
.LBB0_53:
.LBB0_54:
	s_mul_i32 s10, s2, 37
.LBB0_55:
	s_andn2_b64 vcc, exec, s[6:7]
	s_cbranch_vccnz .LBB0_58
	s_and_b64 vcc, exec, s[14:15]
	s_cbranch_vccz .LBB0_59
	s_min_i32 s6, s10, 0x3f98
	s_add_i32 s44, s6, 104
	s_cbranch_execz .LBB0_60
	s_branch .LBB0_61

.LBB0_59:
.LBB0_60:
	s_add_i32 s44, s10, 37
